# fused moe2 unit start: per-unit whole-L2 invalidate dropped (no stale ACTB lines can exist after the preceding grid barrier), keeps A tiles shared in L2
# speedup vs baseline: 1.0107x; 1.0107x over previous
.Lfuse_ready:
.Lfuse_ready2:
	s_barrier
	s_lshl_b32 s12, s20, 2
	s_add_i32 s12, s12, 0
	s_add_i32 s12, s12, 0x20b40
	v_mov_b32_e32 v0, s12
	v_mov_b32_e32 v2, v145
	s_mulk_i32 s20, 0x140
	ds_read_b32 v0, v0
	s_mov_b64 s[12:13], s[0:1]
	s_mov_b64 s[22:23], 0
	s_mov_b64 s[24:25], s[4:5]
	v_add3_u32 v144, s20, v159, v2
	s_mul_i32 s14, s2, 5
	v_lshlrev_b64 v[4:5], 10, v[144:145]
	s_lshl_b32 s2, s2, 4
	v_lshl_add_u64 v[4:5], s[12:13], 0, v[4:5]
	v_mov_b32_e32 v101, v145
	s_and_b32 s12, s2, 0xffffff80
	s_and_b32 s2, s14, 7
	v_lshl_add_u64 v[108:109], v[4:5], 0, v[100:101]
	s_lshl_b32 s36, s2, 7
	v_lshl_add_u64 v[16:17], v[108:109], 0, s[36:37]
	s_waitcnt lgkmcnt(0)
	v_ashrrev_i32_e32 v1, 31, v0
	v_add_co_u32_e32 v4, vcc, s70, v16
	v_lshlrev_b64 v[0:1], 22, v[0:1]
	s_ashr_i32 s13, s12, 31
	v_addc_co_u32_e32 v5, vcc, 0, v17, vcc
	v_lshl_add_u64 v[0:1], s[24:25], 0, v[0:1]
	s_lshl_b64 s[22:23], s[12:13], 2
	v_add_co_u32_e32 v8, vcc, s83, v16
	v_lshl_add_u64 v[0:1], v[0:1], 0, s[22:23]
	v_mov_b32_e32 v103, v145
	v_addc_co_u32_e32 v9, vcc, 0, v17, vcc
	v_lshl_add_u64 v[0:1], v[0:1], 0, v[102:103]
	v_ashrrev_i32_e32 v3, 31, v2
	v_add_co_u32_e32 v12, vcc, s3, v16
	v_lshl_add_u64 v[0:1], v[2:3], 2, v[0:1]
	s_nop 0
	v_addc_co_u32_e32 v13, vcc, 0, v17, vcc
	v_lshl_add_u64 v[110:111], v[0:1], 0, s[10:11]
	v_add_u32_e32 v200, s20, v160
	v_mov_b32_e32 v201, v145
	v_lshl_add_u64 v[202:203], v[200:201], 2, s[8:9]
	global_load_dword v190, v[202:203], off
	global_load_dword v192, v[202:203], off offset:64
	global_load_dword v194, v[202:203], off offset:128
	global_load_dword v196, v[202:203], off offset:192
	global_load_dword v198, v[202:203], off offset:256
	global_load_dwordx4 v[0:3], v[16:17], off
	s_nop 0
	global_load_dwordx4 v[4:7], v[4:5], off
	v_add_co_u32_e32 v16, vcc, s53, v16
	s_lshl_b32 s36, s2, 19
	s_nop 0
	v_addc_co_u32_e32 v17, vcc, 0, v17, vcc
	global_load_dwordx4 v[8:11], v[8:9], off
	s_nop 0
	global_load_dwordx4 v[12:15], v[12:13], off
	global_load_dwordx4 v[16:19], v[16:17], off
	v_lshl_add_u64 v[32:33], v[110:111], 0, s[36:37]
	v_add_co_u32_e32 v34, vcc, 0x2000, v32
	s_nop 1
	v_addc_co_u32_e32 v35, vcc, 0, v33, vcc
	v_add_co_u32_e32 v28, vcc, 0x4000, v32
	s_nop 1
	v_addc_co_u32_e32 v29, vcc, 0, v33, vcc
	v_add_co_u32_e32 v30, vcc, 0x6000, v32
	s_nop 1
	v_addc_co_u32_e32 v31, vcc, 0, v33, vcc
	global_load_dwordx4 v[20:23], v[32:33], off
	global_load_dwordx4 v[24:27], v[34:35], off
	global_load_dwordx4 v[32:35], v[30:31], off
	global_load_dwordx4 v[28:31], v[28:29], off
	s_nop 0
	s_add_i32 s2, s14, 1
	s_nop 0
	s_nop 0
	s_nop 0
	s_nop 0
	s_and_b32 s2, s2, 7
	s_nop 0
	s_lshl_b32 s36, s2, 19
	s_nop 0
	s_nop 0
	s_nop 0
	s_nop 0
	s_nop 0
	v_lshl_add_u64 v[124:125], v[110:111], 0, s[36:37]
	v_add_co_u32_e32 v126, vcc, 0x2000, v124
	s_nop 1
	v_addc_co_u32_e32 v127, vcc, 0, v125, vcc
	v_add_co_u32_e32 v120, vcc, 0x4000, v124
	s_nop 1
	v_addc_co_u32_e32 v121, vcc, 0, v125, vcc
	v_add_co_u32_e32 v122, vcc, 0x6000, v124
	s_nop 1
	v_addc_co_u32_e32 v123, vcc, 0, v125, vcc
	global_load_dwordx4 v[112:115], v[124:125], off
	global_load_dwordx4 v[116:119], v[126:127], off
	global_load_dwordx4 v[124:127], v[122:123], off
	global_load_dwordx4 v[120:123], v[120:121], off
	v_add_u32_e32 v101, s66, v164
	s_nop 0
	s_lshl_b32 s36, s2, 7
	s_nop 0
	v_add_u32_e32 v103, s66, v163
	s_nop 0
	v_mov_b32_e32 v64, 0
	s_nop 0
	s_mov_b32 s15, -2
	s_nop 0
	v_mov_b32_e32 v65, v64
	s_nop 0
	v_mov_b32_e32 v66, v64
	s_nop 0
	s_waitcnt vmcnt(0)
	ds_write_b128 v165, v[0:3]
	ds_write_b128 v165, v[4:7] offset:8192
	ds_write_b128 v165, v[8:11] offset:16384
	ds_write_b128 v165, v[12:15] offset:24576
	ds_write_b128 v165, v[16:19] offset:32768
	v_mov_b32_e32 v67, v64
	v_mov_b32_e32 v68, v64
	v_mov_b32_e32 v69, v64
	v_mov_b32_e32 v70, v64
	v_mov_b32_e32 v71, v64
	v_mov_b32_e32 v72, v64
	v_mov_b32_e32 v73, v64
	v_mov_b32_e32 v74, v64
	v_mov_b32_e32 v75, v64
	v_mov_b32_e32 v76, v64
	v_mov_b32_e32 v77, v64
	v_permlane32_swap_b32_e32 v20, v22
	v_permlane32_swap_b32_e32 v21, v23
	v_permlane32_swap_b32_e32 v24, v26
	v_permlane32_swap_b32_e32 v25, v27
	v_permlane32_swap_b32_e32 v28, v30
	v_permlane32_swap_b32_e32 v29, v31
	v_permlane32_swap_b32_e32 v32, v34
	v_permlane32_swap_b32_e32 v33, v35
	v_cvt_pk_bf16_f32 v0, v20, v24
	v_cvt_pk_bf16_f32 v1, v28, v32
	v_cvt_pk_bf16_f32 v2, v22, v26
	v_cvt_pk_bf16_f32 v3, v30, v34
	v_cvt_pk_bf16_f32 v4, v21, v25
	v_cvt_pk_bf16_f32 v5, v29, v33
	v_cvt_pk_bf16_f32 v6, v23, v27
	v_cvt_pk_bf16_f32 v7, v31, v35
	v_mov_b32_e32 v78, v64
	v_mov_b32_e32 v79, v64
	v_mov_b32_e32 v48, v64
	v_mov_b32_e32 v49, v64
	v_mov_b32_e32 v50, v64
	v_mov_b32_e32 v51, v64
	v_mov_b32_e32 v52, v64
	v_mov_b32_e32 v53, v64
	v_mov_b32_e32 v54, v64
	v_mov_b32_e32 v55, v64
	v_mov_b32_e32 v56, v64
	v_mov_b32_e32 v57, v64
	v_mov_b32_e32 v58, v64
	v_mov_b32_e32 v59, v64
	ds_write_b128 v101, v[0:3]
	v_lshl_add_u64 v[0:1], v[108:109], 0, s[36:37]
	v_add_co_u32_e32 v2, vcc, s70, v0
	ds_write_b128 v103, v[4:7]
	s_nop 0
	v_addc_co_u32_e32 v3, vcc, 0, v1, vcc
	global_load_dwordx4 v[80:83], v[0:1], off
	global_load_dwordx4 v[84:87], v[2:3], off
	v_add_co_u32_e32 v2, vcc, s83, v0
	v_mov_b32_e32 v60, v64
	s_nop 0
	v_addc_co_u32_e32 v3, vcc, 0, v1, vcc
	v_add_co_u32_e32 v4, vcc, 0x30000, v0
	v_mov_b32_e32 v61, v64
	s_nop 0
	v_addc_co_u32_e32 v5, vcc, 0, v1, vcc
	v_add_co_u32_e32 v0, vcc, 0x40000, v0
	global_load_dwordx4 v[88:91], v[2:3], off
	global_load_dwordx4 v[92:95], v[4:5], off
	v_addc_co_u32_e32 v1, vcc, 0, v1, vcc
	global_load_dwordx4 v[96:99], v[0:1], off
	v_mov_b32_e32 v62, v64
	v_mov_b32_e32 v63, v64
	v_mov_b32_e32 v32, v64
	v_mov_b32_e32 v33, v64
	v_mov_b32_e32 v34, v64
	v_mov_b32_e32 v35, v64
	v_mov_b32_e32 v36, v64
	v_mov_b32_e32 v37, v64
	v_mov_b32_e32 v38, v64
	v_mov_b32_e32 v39, v64
	v_mov_b32_e32 v40, v64
	v_mov_b32_e32 v41, v64
	v_mov_b32_e32 v42, v64
	v_mov_b32_e32 v43, v64
	v_mov_b32_e32 v44, v64
	v_mov_b32_e32 v45, v64
	v_mov_b32_e32 v46, v64
	v_mov_b32_e32 v47, v64
	v_mov_b32_e32 v16, v64
	v_mov_b32_e32 v17, v64
	v_mov_b32_e32 v18, v64
	v_mov_b32_e32 v19, v64
	v_mov_b32_e32 v20, v64
	v_mov_b32_e32 v21, v64
	v_mov_b32_e32 v22, v64
	v_mov_b32_e32 v23, v64
	v_mov_b32_e32 v24, v64
	v_mov_b32_e32 v25, v64
	v_mov_b32_e32 v26, v64
	v_mov_b32_e32 v27, v64
	v_mov_b32_e32 v28, v64
	v_mov_b32_e32 v29, v64
	v_mov_b32_e32 v30, v64
	v_mov_b32_e32 v31, v64
	v_mov_b32_e32 v0, v64
	v_mov_b32_e32 v1, v64
	v_mov_b32_e32 v2, v64
	v_mov_b32_e32 v3, v64
	v_mov_b32_e32 v4, v64
	v_mov_b32_e32 v5, v64
	v_mov_b32_e32 v6, v64
	v_mov_b32_e32 v7, v64
	v_mov_b32_e32 v8, v64
	v_mov_b32_e32 v9, v64
	v_mov_b32_e32 v10, v64
	v_mov_b32_e32 v11, v64
	v_mov_b32_e32 v12, v64
	v_mov_b32_e32 v13, v64
	v_mov_b32_e32 v14, v64
	v_mov_b32_e32 v15, v64
	s_waitcnt lgkmcnt(0)
	s_barrier
